# mLSTM local: the 12 K/V staging row loads of an item issued together after the gate loads (7 serialized round trips -> 1)
# speedup vs baseline: 1.0084x; 1.0008x over previous
; __device__ __forceinline__ int shl_i(int v, int from_lane) { return __builtin_amdgcn_ds_bpermute(from_lane << 2, v); }
; __device__ __forceinline__ void ph_mlstm_local(const Frame& F, int j) {
;     ...
;             float a = (tid < 128) ? lf[tid] : 0.f;
; #pragma unroll
;             for (int d = 1; d < 64; d <<= 1) { const float o = __builtin_bit_cast(float, shl_i(__builtin_bit_cast(int, a), lane - d)); if (lane >= d) a += o; }
;             if (tid == 63) wl[0] = a;
;             __syncthreads();
;             if (tid >= 64 && tid < 128) a += wl[0];
;             if (tid < 128) bc[tid] = a;
;         }
;     ...
; #pragma unroll
;         for (int i = 0; i < 2; ++i) {
;             const int u = tid + 512 * i;
;             const int sp = ((u >> 8) << 4) | (u & 15), ch = (u >> 4) & 15;
;             const v4u a = *(const v4u*)(HB + (size_t)(t0 + 2 * sp) * 6144 + 1024 + h * 128 + ch * 8);
;             const v4u bq = *(const v4u*)(HB + (size_t)(t0 + 2 * sp + 1) * 6144 + 1024 + h * 128 + ch * 8);
.LBB0_378:
	s_or_b64 exec, exec, s[52:53]
	s_lshl_b32 s98, s50, 8
	s_addk_i32 s98, 0x800
	s_lshl_b32 s99, s50, 9
	s_addk_i32 s99, 0x1000
	s_movk_i32 s100, 0x3000
	v_add_u32_e32 v100, s57, v63
	v_mul_u32_u24_e32 v100, s100, v100
	v_add3_u32 v100, v100, v0, s98
	global_load_dwordx4 v[112:115], v100, s[0:1]
	v_add_u32_e32 v100, 0x3000, v100
	global_load_dwordx4 v[116:119], v100, s[0:1]
	v_add_u32_e32 v100, s57, v64
	v_mul_u32_u24_e32 v100, s100, v100
	v_add3_u32 v100, v100, v0, s98
	global_load_dwordx4 v[120:123], v100, s[0:1]
	v_add_u32_e32 v100, 0x3000, v100
	global_load_dwordx4 v[124:127], v100, s[0:1]
	v_add_u32_e32 v100, s57, v49
	v_mul_u32_u24_e32 v100, s100, v100
	v_add3_u32 v100, v100, v40, s99
	global_load_dwordx4 v[128:131], v100, s[0:1]
	v_add_u32_e32 v100, 0x3000, v100
	global_load_dwordx4 v[132:135], v100, s[0:1]
	v_add_u32_e32 v100, s57, v51
	v_mul_u32_u24_e32 v100, s100, v100
	v_add3_u32 v100, v100, v40, s99
	global_load_dwordx4 v[136:139], v100, s[0:1]
	v_add_u32_e32 v100, 0x3000, v100
	global_load_dwordx4 v[140:143], v100, s[0:1]
	v_add_u32_e32 v100, s57, v53
	v_mul_u32_u24_e32 v100, s100, v100
	v_add3_u32 v100, v100, v40, s99
	global_load_dwordx4 v[144:147], v100, s[0:1]
	v_add_u32_e32 v100, 0x3000, v100
	global_load_dwordx4 v[148:151], v100, s[0:1]
	v_add_u32_e32 v100, s57, v55
	v_mul_u32_u24_e32 v100, s100, v100
	v_add3_u32 v100, v100, v40, s99
	global_load_dwordx4 v[152:155], v100, s[0:1]
	v_add_u32_e32 v100, 0x3000, v100
	global_load_dwordx4 v[156:159], v100, s[0:1]
	v_mov_b32_e32 v2, 0
	s_waitcnt lgkmcnt(0)
	s_barrier
	s_and_saveexec_b64 s[22:23], vcc
	ds_read_b32 v2, v48
	s_or_b64 exec, exec, s[22:23]
	s_waitcnt lgkmcnt(0)
	ds_bpermute_b32 v3, v57, v2
	s_waitcnt lgkmcnt(0)
	v_add_f32_e32 v3, v2, v3
	v_cndmask_b32_e64 v2, v3, v2, s[8:9]
	ds_bpermute_b32 v3, v58, v2
	s_waitcnt lgkmcnt(0)
	v_add_f32_e32 v3, v2, v3
	v_cndmask_b32_e64 v2, v3, v2, s[12:13]
	ds_bpermute_b32 v3, v59, v2
	s_waitcnt lgkmcnt(0)
	v_add_f32_e32 v3, v2, v3
	v_cndmask_b32_e64 v2, v3, v2, s[14:15]
	ds_bpermute_b32 v3, v60, v2
	s_waitcnt lgkmcnt(0)
	v_add_f32_e32 v3, v2, v3
	v_cndmask_b32_e64 v2, v3, v2, s[16:17]
	ds_bpermute_b32 v3, v61, v2
	s_waitcnt lgkmcnt(0)
	v_add_f32_e32 v3, v2, v3
	v_cndmask_b32_e64 v2, v3, v2, s[18:19]
	ds_bpermute_b32 v3, v62, v2
	s_waitcnt lgkmcnt(0)
	v_add_f32_e32 v3, v2, v3
	v_cndmask_b32_e64 v2, v3, v2, s[20:21]
	s_and_saveexec_b64 s[22:23], s[4:5]
	ds_write_b32 v1, v2 offset:1024
	s_or_b64 exec, exec, s[22:23]
	s_waitcnt lgkmcnt(0)
	s_barrier
	s_and_saveexec_b64 s[22:23], s[6:7]
	s_cbranch_execz .LBB0_384
	ds_read_b32 v3, v1 offset:1024
	s_waitcnt lgkmcnt(0)
	v_add_f32_e32 v2, v2, v3

; #define LAS __attribute__((address_space(3)))
; __device__ __forceinline__ unsigned pk2(float lo, float hi) { return __builtin_amdgcn_perm(__builtin_bit_cast(unsigned, hi) + 0x8000u, __builtin_bit_cast(unsigned, lo) + 0x8000u, 0x07060302u); }
; __device__ __forceinline__ void ml_stage_vt(const bf16* HB, int t0, int h, LAS unsigned char* lds, const LAS float* scl, int tid) {
; #pragma unroll
;     for (int i = 0; i < 4; ++i) {
;         const int u = tid + 512 * i;
;         const int sp = ((u >> 9) << 4) | (u & 15), ch = (u >> 4) & 31;
;         const v4u a = *(const v4u*)(HB + (size_t)(t0 + 2 * sp) * 6144 + 2048 + h * 256 + ch * 8);
;         const v4u b = *(const v4u*)(HB + (size_t)(t0 + 2 * sp + 1) * 6144 + 2048 + h * 256 + ch * 8);
;         float fa[8], fb[8]; unpack8(a, fa); unpack8(b, fb);
;         if (scl) { const float s0 = scl[2 * sp], s1 = scl[2 * sp + 1];
; #pragma unroll
;             for (int e = 0; e < 8; ++e) { fa[e] *= s0; fb[e] *= s1; } }
;         LAS unsigned char* vb = lds + ML_V_OFF + (ch * 8) * ML_ROW + sp * 4;
; #pragma unroll
;         for (int e = 0; e < 8; ++e) *(LAS unsigned*)(vb + e * ML_ROW) = pk2(fa[e], fb[e]);
; __device__ __forceinline__ void ph_mlstm_local(const Frame& F, int j) {
;     ...
; #pragma unroll
;         for (int i = 0; i < 2; ++i) {
;             const int u = tid + 512 * i;
;             const int sp = ((u >> 8) << 4) | (u & 15), ch = (u >> 4) & 15;
;             const v4u a = *(const v4u*)(HB + (size_t)(t0 + 2 * sp) * 6144 + 1024 + h * 128 + ch * 8);
;             const v4u bq = *(const v4u*)(HB + (size_t)(t0 + 2 * sp + 1) * 6144 + 1024 + h * 128 + ch * 8);
;             LAS unsigned char* kb = lds + ML_K_OFF + (ch * 8) * ML_ROW + sp * 4;
;             *(LAS unsigned*)(kb + 0 * ML_ROW) = (a.x & 0xffffu) | (bq.x << 16);      *(LAS unsigned*)(kb + 1 * ML_ROW) = (a.x >> 16) | (bq.x & 0xffff0000u);
;             *(LAS unsigned*)(kb + 2 * ML_ROW) = (a.y & 0xffffu) | (bq.y << 16);      *(LAS unsigned*)(kb + 3 * ML_ROW) = (a.y >> 16) | (bq.y & 0xffff0000u);
;             *(LAS unsigned*)(kb + 4 * ML_ROW) = (a.z & 0xffffu) | (bq.z << 16);      *(LAS unsigned*)(kb + 5 * ML_ROW) = (a.z >> 16) | (bq.z & 0xffff0000u);
;             *(LAS unsigned*)(kb + 6 * ML_ROW) = (a.w & 0xffffu) | (bq.w << 16);      *(LAS unsigned*)(kb + 7 * ML_ROW) = (a.w >> 16) | (bq.w & 0xffff0000u);
;         }
.LBB0_396:
	s_or_b64 exec, exec, s[22:23]
	s_lshl_b32 s22, s50, 7
	s_ashr_i32 s23, s22, 31
	v_add_u32_e32 v8, s57, v63
	v_mov_b64_e32 v[2:3], s[0:1]
	s_movk_i32 s49, 0x3000
	v_mad_i64_i32 v[4:5], s[24:25], v8, s49, v[2:3]
	s_lshl_b64 s[22:23], s[22:23], 1
	v_or_b32_e32 v8, 1, v8
	v_lshl_add_u64 v[4:5], v[4:5], 0, s[22:23]
	v_mad_i64_i32 v[8:9], s[24:25], v8, s49, v[2:3]
	v_lshl_add_u64 v[4:5], v[4:5], 0, v[0:1]
	v_lshl_add_u64 v[8:9], v[8:9], 0, s[22:23]
	s_waitcnt lgkmcnt(0)
	s_barrier
	s_waitcnt vmcnt(0)
	v_mov_b32_e32 v4, v112
	v_mov_b32_e32 v5, v113
	v_mov_b32_e32 v6, v114
	v_mov_b32_e32 v7, v115
	v_lshl_add_u64 v[8:9], v[8:9], 0, v[0:1]
	v_mov_b32_e32 v8, v116
	v_mov_b32_e32 v9, v117
	v_mov_b32_e32 v10, v118
	v_mov_b32_e32 v11, v119
	s_mov_b32 s30, 0xffff0000
	v_mov_b32_e32 v41, v1
	v_lshlrev_b64 v[44:45], 16, v[42:43]
	v_lshl_add_u64 v[44:45], v[38:39], 0, v[44:45]
	s_waitcnt vmcnt(1)
	v_and_b32_e32 v12, 0xffff, v4
	v_lshrrev_b32_e32 v4, 16, v4
	s_waitcnt vmcnt(0)
	v_lshl_or_b32 v12, v8, 16, v12
	v_and_or_b32 v4, v8, s30, v4
	v_add_u32_e32 v8, 0x1000, v66
	ds_write2_b32 v8, v12, v4 offset1:68
	v_and_b32_e32 v4, 0xffff, v5
	v_lshrrev_b32_e32 v5, 16, v5
	v_lshl_or_b32 v4, v9, 16, v4
	v_and_or_b32 v5, v9, s30, v5
	ds_write2_b32 v8, v4, v5 offset0:136 offset1:204
	v_and_b32_e32 v4, 0xffff, v6
	v_lshrrev_b32_e32 v5, 16, v6
	v_lshl_or_b32 v4, v10, 16, v4
	v_and_or_b32 v5, v10, s30, v5
	v_add_u32_e32 v6, 0x1400, v66
	ds_write2_b32 v6, v4, v5 offset0:16 offset1:84
	v_and_b32_e32 v4, 0xffff, v7
	v_lshrrev_b32_e32 v5, 16, v7
	v_lshl_or_b32 v4, v11, 16, v4
	v_and_or_b32 v5, v11, s30, v5
	v_add_u32_e32 v8, s57, v64
	ds_write2_b32 v6, v4, v5 offset0:152 offset1:220
	v_mad_i64_i32 v[4:5], s[24:25], v8, s49, v[2:3]
	v_or_b32_e32 v8, 1, v8
	v_lshl_add_u64 v[4:5], v[4:5], 0, s[22:23]
	v_mad_i64_i32 v[8:9], s[24:25], v8, s49, v[2:3]
	v_lshl_add_u64 v[4:5], v[4:5], 0, v[0:1]
	v_lshl_add_u64 v[8:9], v[8:9], 0, s[22:23]
	v_mov_b32_e32 v4, v120
	v_mov_b32_e32 v5, v121
	v_mov_b32_e32 v6, v122
	v_mov_b32_e32 v7, v123
	v_lshl_add_u64 v[8:9], v[8:9], 0, v[0:1]
	v_mov_b32_e32 v8, v124
	v_mov_b32_e32 v9, v125
	v_mov_b32_e32 v10, v126
	v_mov_b32_e32 v11, v127
	s_lshl_b32 s22, s50, 8
	s_ashr_i32 s23, s22, 31
	s_waitcnt vmcnt(1)
	v_and_b32_e32 v12, 0xffff, v4
	v_lshrrev_b32_e32 v4, 16, v4
	s_waitcnt vmcnt(0)
	v_lshl_or_b32 v12, v8, 16, v12
	v_and_or_b32 v4, v8, s30, v4
	v_add_u32_e32 v8, 0x1000, v67
	ds_write2_b32 v8, v12, v4 offset1:68
	v_and_b32_e32 v4, 0xffff, v5
	v_lshrrev_b32_e32 v5, 16, v5
	v_lshl_or_b32 v4, v9, 16, v4
	v_and_or_b32 v5, v9, s30, v5
	ds_write2_b32 v8, v4, v5 offset0:136 offset1:204
	v_and_b32_e32 v4, 0xffff, v6
	v_lshrrev_b32_e32 v5, 16, v6
	v_lshl_or_b32 v4, v10, 16, v4
	v_and_or_b32 v5, v10, s30, v5
	v_add_u32_e32 v6, 0x1400, v67
	ds_write2_b32 v6, v4, v5 offset0:16 offset1:84
	v_and_b32_e32 v4, 0xffff, v7
	v_lshrrev_b32_e32 v5, 16, v7
	v_lshl_or_b32 v4, v11, 16, v4
	v_and_or_b32 v5, v11, s30, v5
	v_add_u32_e32 v8, s57, v49
	ds_write2_b32 v6, v4, v5 offset0:152 offset1:220
	v_mad_i64_i32 v[4:5], s[24:25], v8, s49, v[2:3]
	s_lshl_b64 s[24:25], s[22:23], 1
	s_nop 0
	v_lshl_add_u64 v[4:5], v[4:5], 0, s[24:25]
	v_lshl_add_u64 v[4:5], v[4:5], 0, v[40:41]
	s_movk_i32 s30, 0x1000
	v_add_co_u32_e64 v4, s[22:23], s30, v4
	v_or_b32_e32 v8, 1, v8
	s_nop 0
	v_addc_co_u32_e64 v5, s[22:23], 0, v5, s[22:23]
	v_mad_i64_i32 v[8:9], s[22:23], v8, s49, v[2:3]
	v_mov_b32_e32 v4, v128
	v_mov_b32_e32 v5, v129
	v_mov_b32_e32 v6, v130
	v_mov_b32_e32 v7, v131
	v_lshl_add_u64 v[8:9], v[8:9], 0, s[24:25]
	v_lshl_add_u64 v[8:9], v[8:9], 0, v[40:41]
	v_add_co_u32_e64 v8, s[22:23], s30, v8
	s_nop 1
	v_addc_co_u32_e64 v9, s[22:23], 0, v9, s[22:23]
	v_mov_b32_e32 v8, v132
	v_mov_b32_e32 v9, v133
	v_mov_b32_e32 v10, v134
	v_mov_b32_e32 v11, v135
	s_waitcnt vmcnt(1)
	v_lshlrev_b32_e32 v12, 16, v4
	v_and_b32_e32 v13, 0xffff0000, v4
	v_lshlrev_b32_e32 v14, 16, v5
	v_and_b32_e32 v15, 0xffff0000, v5
	ds_read_b64 v[4:5], v50 offset:1536
	v_lshlrev_b32_e32 v16, 16, v6
	v_and_b32_e32 v6, 0xffff0000, v6
	v_lshlrev_b32_e32 v17, 16, v7
	s_waitcnt vmcnt(0)
	v_lshlrev_b32_e32 v18, 16, v8
	v_and_b32_e32 v7, 0xffff0000, v7
	v_and_b32_e32 v8, 0xffff0000, v8
	v_lshlrev_b32_e32 v19, 16, v9
	v_and_b32_e32 v9, 0xffff0000, v9
	v_lshlrev_b32_e32 v20, 16, v10
	v_and_b32_e32 v10, 0xffff0000, v10
	v_lshlrev_b32_e32 v21, 16, v11
	v_and_b32_e32 v11, 0xffff0000, v11
	s_waitcnt lgkmcnt(0)
	v_mul_f32_e32 v12, v4, v12
	v_mul_f32_e32 v18, v5, v18
	v_mul_f32_e32 v13, v4, v13
	v_mul_f32_e32 v8, v5, v8
	v_mul_f32_e32 v14, v4, v14
	v_mul_f32_e32 v19, v5, v19
	v_mul_f32_e32 v15, v4, v15
	v_mul_f32_e32 v9, v5, v9
	v_mul_f32_e32 v16, v4, v16
	v_mul_f32_e32 v20, v5, v20
	v_mul_f32_e32 v6, v4, v6
	v_mul_f32_e32 v10, v5, v10
	v_mul_f32_e32 v17, v4, v17
	v_mul_f32_e32 v21, v5, v21
	v_mul_f32_e32 v4, v4, v7
	v_mul_f32_e32 v5, v5, v11
	v_add_u32_e32 v7, 0x8000, v18
	v_add_u32_e32 v11, 0x8000, v12
	v_perm_b32 v7, v7, v11, s33
	v_add_u32_e32 v8, 0x8000, v8
	v_add_u32_e32 v11, 0x8000, v13
	v_perm_b32 v8, v8, v11, s33
	v_add_u32_e32 v11, 0x9800, v68
	ds_write2_b32 v11, v7, v8 offset1:68
	v_add_u32_e32 v7, 0x8000, v19
	v_add_u32_e32 v8, 0x8000, v14
	v_perm_b32 v7, v7, v8, s33
	v_add_u32_e32 v8, 0x8000, v9
	v_add_u32_e32 v9, 0x8000, v15
	v_perm_b32 v8, v8, v9, s33
	ds_write2_b32 v11, v7, v8 offset0:136 offset1:204
	v_add_u32_e32 v7, 0x8000, v20
	v_add_u32_e32 v8, 0x8000, v16
	v_perm_b32 v7, v7, v8, s33
	v_add_u32_e32 v8, 0x8000, v10
	v_add_u32_e32 v6, 0x8000, v6
	v_perm_b32 v6, v8, v6, s33
	v_add_u32_e32 v8, 0x9c00, v68
	ds_write2_b32 v8, v7, v6 offset0:16 offset1:84
	v_add_u32_e32 v6, 0x8000, v21
	v_add_u32_e32 v7, 0x8000, v17
	v_add_u32_e32 v5, 0x8000, v5
	v_add_u32_e32 v4, 0x8000, v4
	v_perm_b32 v6, v6, v7, s33
	v_perm_b32 v4, v5, v4, s33
	ds_write2_b32 v8, v6, v4 offset0:152 offset1:220
	v_add_u32_e32 v8, s57, v51
	v_mad_i64_i32 v[4:5], s[22:23], v8, s49, v[2:3]
	v_lshl_add_u64 v[4:5], v[4:5], 0, s[24:25]
	v_lshl_add_u64 v[4:5], v[4:5], 0, v[40:41]
	v_add_co_u32_e64 v4, s[22:23], s30, v4
	v_or_b32_e32 v8, 1, v8
	s_nop 0
	v_addc_co_u32_e64 v5, s[22:23], 0, v5, s[22:23]
	v_mad_i64_i32 v[8:9], s[22:23], v8, s49, v[2:3]
	v_mov_b32_e32 v4, v136
	v_mov_b32_e32 v5, v137
	v_mov_b32_e32 v6, v138
	v_mov_b32_e32 v7, v139
	v_lshl_add_u64 v[8:9], v[8:9], 0, s[24:25]
	v_lshl_add_u64 v[8:9], v[8:9], 0, v[40:41]
	v_add_co_u32_e64 v8, s[22:23], s30, v8
	s_nop 1
	v_addc_co_u32_e64 v9, s[22:23], 0, v9, s[22:23]
	v_mov_b32_e32 v8, v140
	v_mov_b32_e32 v9, v141
	v_mov_b32_e32 v10, v142
	v_mov_b32_e32 v11, v143
	s_waitcnt vmcnt(1)
; #define LAS __attribute__((address_space(3)))
; __device__ __forceinline__ unsigned pk2(float lo, float hi) { return __builtin_amdgcn_perm(__builtin_bit_cast(unsigned, hi) + 0x8000u, __builtin_bit_cast(unsigned, lo) + 0x8000u, 0x07060302u); }
; __device__ __forceinline__ void ml_stage_vt(const bf16* HB, int t0, int h, LAS unsigned char* lds, const LAS float* scl, int tid) {
; #pragma unroll
;     for (int i = 0; i < 4; ++i) {
;         const int u = tid + 512 * i;
;         const int sp = ((u >> 9) << 4) | (u & 15), ch = (u >> 4) & 31;
;         const v4u a = *(const v4u*)(HB + (size_t)(t0 + 2 * sp) * 6144 + 2048 + h * 256 + ch * 8);
;         const v4u b = *(const v4u*)(HB + (size_t)(t0 + 2 * sp + 1) * 6144 + 2048 + h * 256 + ch * 8);
;         float fa[8], fb[8]; unpack8(a, fa); unpack8(b, fb);
;         if (scl) { const float s0 = scl[2 * sp], s1 = scl[2 * sp + 1];
; #pragma unroll
;             for (int e = 0; e < 8; ++e) { fa[e] *= s0; fb[e] *= s1; } }
;         LAS unsigned char* vb = lds + ML_V_OFF + (ch * 8) * ML_ROW + sp * 4;
; #pragma unroll
;         for (int e = 0; e < 8; ++e) *(LAS unsigned*)(vb + e * ML_ROW) = pk2(fa[e], fb[e]);
	v_lshlrev_b32_e32 v12, 16, v4
	v_and_b32_e32 v13, 0xffff0000, v4
	v_lshlrev_b32_e32 v14, 16, v5
	v_and_b32_e32 v15, 0xffff0000, v5
	ds_read_b64 v[4:5], v52 offset:1536
	v_lshlrev_b32_e32 v16, 16, v6
	v_and_b32_e32 v6, 0xffff0000, v6
	v_lshlrev_b32_e32 v17, 16, v7
	s_waitcnt vmcnt(0)
	v_lshlrev_b32_e32 v18, 16, v8
	v_and_b32_e32 v7, 0xffff0000, v7
	v_and_b32_e32 v8, 0xffff0000, v8
	v_lshlrev_b32_e32 v19, 16, v9
	v_and_b32_e32 v9, 0xffff0000, v9
	v_lshlrev_b32_e32 v20, 16, v10
	v_and_b32_e32 v10, 0xffff0000, v10
	v_lshlrev_b32_e32 v21, 16, v11
	v_and_b32_e32 v11, 0xffff0000, v11
	s_waitcnt lgkmcnt(0)
	v_mul_f32_e32 v12, v4, v12
	v_mul_f32_e32 v18, v5, v18
	v_mul_f32_e32 v13, v4, v13
	v_mul_f32_e32 v8, v5, v8
	v_mul_f32_e32 v14, v4, v14
	v_mul_f32_e32 v19, v5, v19
	v_mul_f32_e32 v15, v4, v15
	v_mul_f32_e32 v9, v5, v9
	v_mul_f32_e32 v16, v4, v16
	v_mul_f32_e32 v20, v5, v20
	v_mul_f32_e32 v6, v4, v6
	v_mul_f32_e32 v10, v5, v10
	v_mul_f32_e32 v17, v4, v17
	v_mul_f32_e32 v21, v5, v21
	v_mul_f32_e32 v4, v4, v7
	v_mul_f32_e32 v5, v5, v11
	v_add_u32_e32 v7, 0x8000, v18
	v_add_u32_e32 v11, 0x8000, v12
	v_perm_b32 v7, v7, v11, s33
	v_add_u32_e32 v8, 0x8000, v8
	v_add_u32_e32 v11, 0x8000, v13
	v_perm_b32 v8, v8, v11, s33
	v_add_u32_e32 v11, 0x9800, v69
	ds_write2_b32 v11, v7, v8 offset1:68
	v_add_u32_e32 v7, 0x8000, v19
	v_add_u32_e32 v8, 0x8000, v14
	v_perm_b32 v7, v7, v8, s33
	v_add_u32_e32 v8, 0x8000, v9
	v_add_u32_e32 v9, 0x8000, v15
	v_perm_b32 v8, v8, v9, s33
	ds_write2_b32 v11, v7, v8 offset0:136 offset1:204
	v_add_u32_e32 v7, 0x8000, v20
	v_add_u32_e32 v8, 0x8000, v16
	v_perm_b32 v7, v7, v8, s33
	v_add_u32_e32 v8, 0x8000, v10
	v_add_u32_e32 v6, 0x8000, v6
	v_perm_b32 v6, v8, v6, s33
	v_add_u32_e32 v8, 0x9c00, v69
	ds_write2_b32 v8, v7, v6 offset0:16 offset1:84
	v_add_u32_e32 v6, 0x8000, v21
	v_add_u32_e32 v7, 0x8000, v17
	v_add_u32_e32 v5, 0x8000, v5
	v_add_u32_e32 v4, 0x8000, v4
	v_perm_b32 v6, v6, v7, s33
	v_perm_b32 v4, v5, v4, s33
	ds_write2_b32 v8, v6, v4 offset0:152 offset1:220
	v_add_u32_e32 v8, s57, v53
	v_mad_i64_i32 v[4:5], s[22:23], v8, s49, v[2:3]
	v_lshl_add_u64 v[4:5], v[4:5], 0, s[24:25]
	v_lshl_add_u64 v[4:5], v[4:5], 0, v[40:41]
	v_add_co_u32_e64 v4, s[22:23], s30, v4
	v_or_b32_e32 v8, 1, v8
	s_nop 0
	v_addc_co_u32_e64 v5, s[22:23], 0, v5, s[22:23]
	v_mad_i64_i32 v[8:9], s[22:23], v8, s49, v[2:3]
	v_mov_b32_e32 v4, v144
	v_mov_b32_e32 v5, v145
	v_mov_b32_e32 v6, v146
	v_mov_b32_e32 v7, v147
	v_lshl_add_u64 v[8:9], v[8:9], 0, s[24:25]
	v_lshl_add_u64 v[8:9], v[8:9], 0, v[40:41]
	v_add_co_u32_e64 v8, s[22:23], s30, v8
	s_nop 1
	v_addc_co_u32_e64 v9, s[22:23], 0, v9, s[22:23]
	v_mov_b32_e32 v8, v148
	v_mov_b32_e32 v9, v149
	v_mov_b32_e32 v10, v150
	v_mov_b32_e32 v11, v151
	s_waitcnt vmcnt(1)
	v_lshlrev_b32_e32 v12, 16, v4
	v_and_b32_e32 v13, 0xffff0000, v4
	v_lshlrev_b32_e32 v14, 16, v5
	v_and_b32_e32 v15, 0xffff0000, v5
	ds_read_b64 v[4:5], v54 offset:1536
	v_lshlrev_b32_e32 v16, 16, v6
	v_and_b32_e32 v6, 0xffff0000, v6
	v_lshlrev_b32_e32 v17, 16, v7
	s_waitcnt vmcnt(0)
	v_lshlrev_b32_e32 v18, 16, v8
	v_and_b32_e32 v7, 0xffff0000, v7
	v_and_b32_e32 v8, 0xffff0000, v8
	v_lshlrev_b32_e32 v19, 16, v9
	v_and_b32_e32 v9, 0xffff0000, v9
	v_lshlrev_b32_e32 v20, 16, v10
	v_and_b32_e32 v10, 0xffff0000, v10
	v_lshlrev_b32_e32 v21, 16, v11
	v_and_b32_e32 v11, 0xffff0000, v11
	s_waitcnt lgkmcnt(0)
	v_mul_f32_e32 v12, v4, v12
	v_mul_f32_e32 v18, v5, v18
	v_mul_f32_e32 v13, v4, v13
	v_mul_f32_e32 v8, v5, v8
	v_mul_f32_e32 v14, v4, v14
	v_mul_f32_e32 v19, v5, v19
	v_mul_f32_e32 v15, v4, v15
	v_mul_f32_e32 v9, v5, v9
	v_mul_f32_e32 v16, v4, v16
	v_mul_f32_e32 v20, v5, v20
	v_mul_f32_e32 v6, v4, v6
	v_mul_f32_e32 v10, v5, v10
	v_mul_f32_e32 v17, v4, v17
	v_mul_f32_e32 v21, v5, v21
	v_mul_f32_e32 v4, v4, v7
	v_mul_f32_e32 v5, v5, v11
	v_add_u32_e32 v7, 0x8000, v18
	v_add_u32_e32 v11, 0x8000, v12
	v_perm_b32 v7, v7, v11, s33
	v_add_u32_e32 v8, 0x8000, v8
	v_add_u32_e32 v11, 0x8000, v13
	v_perm_b32 v8, v8, v11, s33
	v_add_u32_e32 v11, 0x9800, v70
	ds_write2_b32 v11, v7, v8 offset1:68
	v_add_u32_e32 v7, 0x8000, v19
	v_add_u32_e32 v8, 0x8000, v14
	v_perm_b32 v7, v7, v8, s33
	v_add_u32_e32 v8, 0x8000, v9
	v_add_u32_e32 v9, 0x8000, v15
	v_perm_b32 v8, v8, v9, s33
	ds_write2_b32 v11, v7, v8 offset0:136 offset1:204
	v_add_u32_e32 v7, 0x8000, v20
	v_add_u32_e32 v8, 0x8000, v16
	v_perm_b32 v7, v7, v8, s33
	v_add_u32_e32 v8, 0x8000, v10
	v_add_u32_e32 v6, 0x8000, v6
	v_perm_b32 v6, v8, v6, s33
	v_add_u32_e32 v8, 0x9c00, v70
	ds_write2_b32 v8, v7, v6 offset0:16 offset1:84
	v_add_u32_e32 v6, 0x8000, v21
	v_add_u32_e32 v7, 0x8000, v17
	v_add_u32_e32 v5, 0x8000, v5
	v_add_u32_e32 v4, 0x8000, v4
	v_perm_b32 v6, v6, v7, s33
	v_perm_b32 v4, v5, v4, s33
	ds_write2_b32 v8, v6, v4 offset0:152 offset1:220
	v_add_u32_e32 v6, s57, v55
	v_mad_i64_i32 v[4:5], s[22:23], v6, s49, v[2:3]
	v_lshl_add_u64 v[4:5], v[4:5], 0, s[24:25]
	v_lshl_add_u64 v[4:5], v[4:5], 0, v[40:41]
	v_add_co_u32_e64 v4, s[22:23], s30, v4
	s_nop 1
	v_addc_co_u32_e64 v5, s[22:23], 0, v5, s[22:23]
	v_mov_b32_e32 v12, v152
	v_mov_b32_e32 v13, v153
	v_mov_b32_e32 v14, v154
	v_mov_b32_e32 v15, v155
	v_or_b32_e32 v4, 1, v6
	v_mad_i64_i32 v[2:3], s[22:23], v4, s49, v[2:3]
	v_lshl_add_u64 v[2:3], v[2:3], 0, s[24:25]
	v_lshl_add_u64 v[2:3], v[2:3], 0, v[40:41]
	v_add_co_u32_e64 v2, s[22:23], s30, v2
	s_waitcnt vmcnt(0)
	v_lshlrev_b32_e32 v11, 16, v12
	v_addc_co_u32_e64 v3, s[22:23], 0, v3, s[22:23]
	v_mov_b32_e32 v20, v156
	v_mov_b32_e32 v21, v157
	v_mov_b32_e32 v22, v158
	v_mov_b32_e32 v23, v159
	ds_read_b64 v[2:3], v56 offset:1536
	v_and_b32_e32 v10, 0xffff0000, v12
	v_lshlrev_b32_e32 v9, 16, v13
	v_and_b32_e32 v8, 0xffff0000, v13
	v_lshlrev_b32_e32 v7, 16, v14
	v_and_b32_e32 v6, 0xffff0000, v14
	v_lshlrev_b32_e32 v5, 16, v15
	v_and_b32_e32 v4, 0xffff0000, v15
	s_waitcnt lgkmcnt(0)
; #define LAS __attribute__((address_space(3)))
; __device__ __forceinline__ unsigned pk2(float lo, float hi) { return __builtin_amdgcn_perm(__builtin_bit_cast(unsigned, hi) + 0x8000u, __builtin_bit_cast(unsigned, lo) + 0x8000u, 0x07060302u); }
; __device__ __forceinline__ void ml_stage_vt(const bf16* HB, int t0, int h, LAS unsigned char* lds, const LAS float* scl, int tid) {
;     ...
;             for (int e = 0; e < 8; ++e) { fa[e] *= s0; fb[e] *= s1; } }
;         LAS unsigned char* vb = lds + ML_V_OFF + (ch * 8) * ML_ROW + sp * 4;
; #pragma unroll
;         for (int e = 0; e < 8; ++e) *(LAS unsigned*)(vb + e * ML_ROW) = pk2(fa[e], fb[e]);
; __device__ __forceinline__ void ph_mlstm_local(const Frame& F, int j) {
;     ...
;         bf16x8 bfr[2][4];
; #pragma unroll
;         for (int vt = 0; vt < 2; ++vt)
; #pragma unroll
;             for (int st = 0; st < 4; ++st) bfr[vt][st] = *(const LAS bf16x8*)(lds + ML_V_OFF + (16 * (2 * wave + vt) + l15) * ML_ROW + 16 * g + 64 * st);
; #pragma unroll
;         for (int kt = 0; kt < 8; ++kt) {
;             f32x4 c0 = (f32x4){0.f, 0.f, 0.f, 0.f}, c1 = (f32x4){0.f, 0.f, 0.f, 0.f};
; #pragma unroll
;             for (int st = 0; st < 4; ++st) {
;                 const bf16x8 af = *(const LAS bf16x8*)(lds + ML_K_OFF + (16 * kt + l15) * ML_ROW + 16 * g + 64 * st);
;                 c0 = __builtin_amdgcn_mfma_f32_16x16x32_bf16(af, bfr[0][st], c0, 0, 0, 0);
;                 c1 = __builtin_amdgcn_mfma_f32_16x16x32_bf16(af, bfr[1][st], c1, 0, 0, 0);
;             }
;             bf16* cp = CLOC + ((size_t)item * 256 + 16 * (2 * wave) + l15) * 128 + 16 * kt + 4 * g;
;             v2u w0; w0.x = pk2(c0[0], c0[1]); w0.y = pk2(c0[2], c0[3]); *(v2u*)cp = w0;
;             v2u w1; w1.x = pk2(c1[0], c1[1]); w1.y = pk2(c1[2], c1[3]); *(v2u*)(cp + 16 * 128) = w1;
;         }
	v_mul_f32_e32 v11, v2, v11
	v_mul_f32_e32 v10, v2, v10
	v_mul_f32_e32 v9, v2, v9
	v_mul_f32_e32 v8, v2, v8
	v_mul_f32_e32 v7, v2, v7
	v_mul_f32_e32 v6, v2, v6
	v_mul_f32_e32 v5, v2, v5
	v_mul_f32_e32 v2, v2, v4
	v_add_u32_e32 v11, 0x8000, v11
	v_add_u32_e32 v10, 0x8000, v10
	v_add_u32_e32 v9, 0x8000, v9
	v_add_u32_e32 v8, 0x8000, v8
	v_add_u32_e32 v7, 0x8000, v7
	v_add_u32_e32 v6, 0x8000, v6
	v_add_u32_e32 v5, 0x8000, v5
	v_add_u32_e32 v2, 0x8000, v2
	s_waitcnt vmcnt(0)
	v_lshlrev_b32_e32 v19, 16, v20
	v_and_b32_e32 v18, 0xffff0000, v20
	v_mul_f32_e32 v19, v3, v19
	v_mul_f32_e32 v18, v3, v18
	v_add_u32_e32 v4, 0x8000, v19
	v_lshlrev_b32_e32 v17, 16, v21
	v_perm_b32 v4, v4, v11, s33
	v_add_u32_e32 v11, 0x8000, v18
	v_and_b32_e32 v16, 0xffff0000, v21
	v_mul_f32_e32 v17, v3, v17
	v_perm_b32 v10, v11, v10, s33
	v_add_u32_e32 v11, 0x9800, v71
	v_mul_f32_e32 v16, v3, v16
	ds_write2_b32 v11, v4, v10 offset1:68
	v_add_u32_e32 v4, 0x8000, v17
	v_lshlrev_b32_e32 v15, 16, v22
	v_perm_b32 v4, v4, v9, s33
	v_add_u32_e32 v9, 0x8000, v16
	v_and_b32_e32 v14, 0xffff0000, v22
	v_mul_f32_e32 v15, v3, v15
	v_perm_b32 v8, v9, v8, s33
	v_mul_f32_e32 v14, v3, v14
	ds_write2_b32 v11, v4, v8 offset0:136 offset1:204
	v_add_u32_e32 v4, 0x8000, v15
	v_lshlrev_b32_e32 v13, 16, v23
	v_and_b32_e32 v12, 0xffff0000, v23
	v_perm_b32 v4, v4, v7, s33
	v_add_u32_e32 v7, 0x8000, v14
	v_mul_f32_e32 v13, v3, v13
	v_mul_f32_e32 v3, v3, v12
	v_perm_b32 v6, v7, v6, s33
	v_add_u32_e32 v7, 0x9c00, v71
	ds_write2_b32 v7, v4, v6 offset0:16 offset1:84
	v_add_u32_e32 v4, 0x8000, v13
	v_add_u32_e32 v3, 0x8000, v3
	v_perm_b32 v4, v4, v5, s33
	v_perm_b32 v2, v3, v2, s33
	ds_write2_b32 v7, v4, v2 offset0:152 offset1:220
	s_waitcnt lgkmcnt(0)
	s_barrier
	ds_read_b128 v[26:29], v72 offset:38912
	ds_read_b128 v[18:21], v72 offset:38976
	ds_read_b128 v[10:13], v72 offset:39040
	ds_read_b128 v[6:9], v72 offset:39104
	ds_read_b128 v[30:33], v72 offset:43264
	ds_read_b128 v[22:25], v72 offset:43328
	ds_read_b128 v[14:17], v72 offset:43392
	ds_read_b128 v[2:5], v72 offset:43456
	ds_read_b128 v[74:77], v73 offset:4096
	ds_read_b128 v[82:85], v73 offset:4160
	s_waitcnt lgkmcnt(1)
	v_mfma_f32_16x16x32_bf16 v[78:81], v[74:77], v[26:29], 0
	v_mfma_f32_16x16x32_bf16 v[74:77], v[74:77], v[30:33], 0
	s_waitcnt lgkmcnt(0)
	v_mfma_f32_16x16x32_bf16 v[78:81], v[82:85], v[18:21], v[78:81]
	v_mfma_f32_16x16x32_bf16 v[74:77], v[82:85], v[22:25], v[74:77]
	ds_read_b128 v[82:85], v73 offset:4224
	s_waitcnt lgkmcnt(0)
	v_mfma_f32_16x16x32_bf16 v[78:81], v[82:85], v[10:13], v[78:81]
	v_mfma_f32_16x16x32_bf16 v[74:77], v[82:85], v[14:17], v[74:77]
	ds_read_b128 v[82:85], v73 offset:4288
	s_waitcnt lgkmcnt(0)
	v_mfma_f32_16x16x32_bf16 v[78:81], v[82:85], v[6:9], v[78:81]
	s_nop 7
	v_add_u32_e32 v41, 0x8000, v79
	v_mfma_f32_16x16x32_bf16 v[74:77], v[82:85], v[2:5], v[74:77]
	v_add_u32_e32 v46, 0x8000, v78
	v_perm_b32 v46, v41, v46, s33
	v_add_u32_e32 v41, 0x8000, v81
	v_add_u32_e32 v47, 0x8000, v80
	v_perm_b32 v47, v41, v47, s33
	global_store_dwordx2 v[44:45], v[46:47], off
	s_nop 1
	v_add_u32_e32 v41, 0x8000, v75
	v_add_u32_e32 v46, 0x8000, v74
	v_perm_b32 v74, v41, v46, s33
	v_add_u32_e32 v41, 0x8000, v77
	v_add_u32_e32 v46, 0x8000, v76
	v_perm_b32 v75, v41, v46, s33
	v_add_co_u32_e64 v46, s[22:23], s30, v44
	ds_read_b128 v[82:85], v73 offset:8512
	s_nop 0
	v_addc_co_u32_e64 v47, s[22:23], 0, v45, s[22:23]
	global_store_dwordx2 v[46:47], v[74:75], off
	ds_read_b128 v[74:77], v73 offset:8448
	s_waitcnt lgkmcnt(0)
	v_mfma_f32_16x16x32_bf16 v[78:81], v[74:77], v[26:29], 0
	v_mfma_f32_16x16x32_bf16 v[74:77], v[74:77], v[30:33], 0
	v_mfma_f32_16x16x32_bf16 v[78:81], v[82:85], v[18:21], v[78:81]
	v_mfma_f32_16x16x32_bf16 v[74:77], v[82:85], v[22:25], v[74:77]
	ds_read_b128 v[82:85], v73 offset:8576
	s_waitcnt lgkmcnt(0)
	v_mfma_f32_16x16x32_bf16 v[78:81], v[82:85], v[10:13], v[78:81]
	v_mfma_f32_16x16x32_bf16 v[74:77], v[82:85], v[14:17], v[74:77]
	ds_read_b128 v[82:85], v73 offset:8640
	s_waitcnt lgkmcnt(0)
	v_mfma_f32_16x16x32_bf16 v[78:81], v[82:85], v[6:9], v[78:81]
	s_nop 7
	v_add_u32_e32 v41, 0x8000, v79
	v_mfma_f32_16x16x32_bf16 v[74:77], v[82:85], v[2:5], v[74:77]
	v_add_u32_e32 v78, 0x8000, v78
	v_perm_b32 v78, v41, v78, s33
	v_add_u32_e32 v41, 0x8000, v81
	v_add_u32_e32 v79, 0x8000, v80
	v_perm_b32 v79, v41, v79, s33
	s_nop 2
	v_add_u32_e32 v41, 0x8000, v75
	v_add_u32_e32 v74, 0x8000, v74
	v_perm_b32 v74, v41, v74, s33
	v_add_u32_e32 v41, 0x8000, v77
	v_add_u32_e32 v75, 0x8000, v76
	v_perm_b32 v75, v41, v75, s33
	global_store_dwordx2 v[46:47], v[74:75], off offset:32
	ds_read_b128 v[74:77], v73 offset:12800
	ds_read_b128 v[82:85], v73 offset:12864
	global_store_dwordx2 v[44:45], v[78:79], off offset:32
	s_waitcnt lgkmcnt(1)
	v_mfma_f32_16x16x32_bf16 v[78:81], v[74:77], v[26:29], 0
	v_mfma_f32_16x16x32_bf16 v[74:77], v[74:77], v[30:33], 0
	s_waitcnt lgkmcnt(0)
	v_mfma_f32_16x16x32_bf16 v[78:81], v[82:85], v[18:21], v[78:81]
	v_mfma_f32_16x16x32_bf16 v[74:77], v[82:85], v[22:25], v[74:77]
	ds_read_b128 v[82:85], v73 offset:12928
	s_waitcnt lgkmcnt(0)
	v_mfma_f32_16x16x32_bf16 v[78:81], v[82:85], v[10:13], v[78:81]
	v_mfma_f32_16x16x32_bf16 v[74:77], v[82:85], v[14:17], v[74:77]
	ds_read_b128 v[82:85], v73 offset:12992
	s_waitcnt lgkmcnt(0)
	v_mfma_f32_16x16x32_bf16 v[78:81], v[82:85], v[6:9], v[78:81]
	s_nop 7
	v_add_u32_e32 v41, 0x8000, v79
	v_mfma_f32_16x16x32_bf16 v[74:77], v[82:85], v[2:5], v[74:77]
	v_add_u32_e32 v78, 0x8000, v78
	v_perm_b32 v78, v41, v78, s33
	v_add_u32_e32 v41, 0x8000, v81
	v_add_u32_e32 v79, 0x8000, v80
	v_perm_b32 v79, v41, v79, s33
	s_nop 2
	v_add_u32_e32 v41, 0x8000, v75
	v_add_u32_e32 v74, 0x8000, v74
	v_perm_b32 v74, v41, v74, s33
	v_add_u32_e32 v41, 0x8000, v77
	v_add_u32_e32 v75, 0x8000, v76
	v_perm_b32 v75, v41, v75, s33
	global_store_dwordx2 v[46:47], v[74:75], off offset:64
	ds_read_b128 v[74:77], v73 offset:17152
	ds_read_b128 v[82:85], v73 offset:17216
	global_store_dwordx2 v[44:45], v[78:79], off offset:64
	s_waitcnt lgkmcnt(1)
; #define LAS __attribute__((address_space(3)))
; __device__ __forceinline__ unsigned pk2(float lo, float hi) { return __builtin_amdgcn_perm(__builtin_bit_cast(unsigned, hi) + 0x8000u, __builtin_bit_cast(unsigned, lo) + 0x8000u, 0x07060302u); }
; __device__ __forceinline__ void ph_mlstm_local(const Frame& F, int j) {
;     ...
;         for (int kt = 0; kt < 8; ++kt) {
;             f32x4 c0 = (f32x4){0.f, 0.f, 0.f, 0.f}, c1 = (f32x4){0.f, 0.f, 0.f, 0.f};
; #pragma unroll
;             for (int st = 0; st < 4; ++st) {
;                 const bf16x8 af = *(const LAS bf16x8*)(lds + ML_K_OFF + (16 * kt + l15) * ML_ROW + 16 * g + 64 * st);
;                 c0 = __builtin_amdgcn_mfma_f32_16x16x32_bf16(af, bfr[0][st], c0, 0, 0, 0);
;                 c1 = __builtin_amdgcn_mfma_f32_16x16x32_bf16(af, bfr[1][st], c1, 0, 0, 0);
;             }
;             bf16* cp = CLOC + ((size_t)item * 256 + 16 * (2 * wave) + l15) * 128 + 16 * kt + 4 * g;
;             v2u w0; w0.x = pk2(c0[0], c0[1]); w0.y = pk2(c0[2], c0[3]); *(v2u*)cp = w0;
;             v2u w1; w1.x = pk2(c1[0], c1[1]); w1.y = pk2(c1[2], c1[3]); *(v2u*)(cp + 16 * 128) = w1;
;         }
;         if (tid < 128) {
;             float n = 0.f;
;             const LAS unsigned* kr = (const LAS unsigned*)(lds + ML_K_OFF + tid * ML_ROW);
	v_mfma_f32_16x16x32_bf16 v[78:81], v[74:77], v[26:29], 0
	v_mfma_f32_16x16x32_bf16 v[74:77], v[74:77], v[30:33], 0
	s_waitcnt lgkmcnt(0)
	v_mfma_f32_16x16x32_bf16 v[78:81], v[82:85], v[18:21], v[78:81]
	v_mfma_f32_16x16x32_bf16 v[74:77], v[82:85], v[22:25], v[74:77]
	ds_read_b128 v[82:85], v73 offset:17280
	s_waitcnt lgkmcnt(0)
	v_mfma_f32_16x16x32_bf16 v[78:81], v[82:85], v[10:13], v[78:81]
	v_mfma_f32_16x16x32_bf16 v[74:77], v[82:85], v[14:17], v[74:77]
	ds_read_b128 v[82:85], v73 offset:17344
	s_waitcnt lgkmcnt(0)
	v_mfma_f32_16x16x32_bf16 v[78:81], v[82:85], v[6:9], v[78:81]
	s_nop 7
	v_add_u32_e32 v41, 0x8000, v79
	v_mfma_f32_16x16x32_bf16 v[74:77], v[82:85], v[2:5], v[74:77]
	v_add_u32_e32 v78, 0x8000, v78
	v_perm_b32 v78, v41, v78, s33
	v_add_u32_e32 v41, 0x8000, v81
	v_add_u32_e32 v79, 0x8000, v80
	v_perm_b32 v79, v41, v79, s33
	s_nop 2
	v_add_u32_e32 v41, 0x8000, v75
	v_add_u32_e32 v74, 0x8000, v74
	v_perm_b32 v74, v41, v74, s33
	v_add_u32_e32 v41, 0x8000, v77
	v_add_u32_e32 v75, 0x8000, v76
	v_perm_b32 v75, v41, v75, s33
	global_store_dwordx2 v[46:47], v[74:75], off offset:96
	ds_read_b128 v[74:77], v73 offset:21504
	ds_read_b128 v[82:85], v73 offset:21568
	global_store_dwordx2 v[44:45], v[78:79], off offset:96
	s_waitcnt lgkmcnt(1)
	v_mfma_f32_16x16x32_bf16 v[78:81], v[74:77], v[26:29], 0
	v_mfma_f32_16x16x32_bf16 v[74:77], v[74:77], v[30:33], 0
	s_waitcnt lgkmcnt(0)
	v_mfma_f32_16x16x32_bf16 v[78:81], v[82:85], v[18:21], v[78:81]
	v_mfma_f32_16x16x32_bf16 v[74:77], v[82:85], v[22:25], v[74:77]
	ds_read_b128 v[82:85], v73 offset:21632
	s_waitcnt lgkmcnt(0)
	v_mfma_f32_16x16x32_bf16 v[78:81], v[82:85], v[10:13], v[78:81]
	v_mfma_f32_16x16x32_bf16 v[74:77], v[82:85], v[14:17], v[74:77]
	ds_read_b128 v[82:85], v73 offset:21696
	s_waitcnt lgkmcnt(0)
	v_mfma_f32_16x16x32_bf16 v[78:81], v[82:85], v[6:9], v[78:81]
	s_nop 7
	v_add_u32_e32 v41, 0x8000, v79
	v_mfma_f32_16x16x32_bf16 v[74:77], v[82:85], v[2:5], v[74:77]
	v_add_u32_e32 v78, 0x8000, v78
	v_perm_b32 v78, v41, v78, s33
	v_add_u32_e32 v41, 0x8000, v81
	v_add_u32_e32 v79, 0x8000, v80
	v_perm_b32 v79, v41, v79, s33
	s_nop 2
	v_add_u32_e32 v41, 0x8000, v75
	v_add_u32_e32 v74, 0x8000, v74
	v_perm_b32 v74, v41, v74, s33
	v_add_u32_e32 v41, 0x8000, v77
	v_add_u32_e32 v75, 0x8000, v76
	v_perm_b32 v75, v41, v75, s33
	global_store_dwordx2 v[46:47], v[74:75], off offset:128
	ds_read_b128 v[74:77], v73 offset:25856
	ds_read_b128 v[82:85], v73 offset:25920
	global_store_dwordx2 v[44:45], v[78:79], off offset:128
	s_waitcnt lgkmcnt(1)
	v_mfma_f32_16x16x32_bf16 v[78:81], v[74:77], v[26:29], 0
	v_mfma_f32_16x16x32_bf16 v[74:77], v[74:77], v[30:33], 0
	s_waitcnt lgkmcnt(0)
	v_mfma_f32_16x16x32_bf16 v[78:81], v[82:85], v[18:21], v[78:81]
	v_mfma_f32_16x16x32_bf16 v[74:77], v[82:85], v[22:25], v[74:77]
	ds_read_b128 v[82:85], v73 offset:25984
	s_waitcnt lgkmcnt(0)
	v_mfma_f32_16x16x32_bf16 v[78:81], v[82:85], v[10:13], v[78:81]
	v_mfma_f32_16x16x32_bf16 v[74:77], v[82:85], v[14:17], v[74:77]
	ds_read_b128 v[82:85], v73 offset:26048
	s_waitcnt lgkmcnt(0)
	v_mfma_f32_16x16x32_bf16 v[78:81], v[82:85], v[6:9], v[78:81]
	s_nop 7
	v_add_u32_e32 v41, 0x8000, v79
	v_mfma_f32_16x16x32_bf16 v[74:77], v[82:85], v[2:5], v[74:77]
	v_add_u32_e32 v78, 0x8000, v78
	v_perm_b32 v78, v41, v78, s33
	v_add_u32_e32 v41, 0x8000, v81
	v_add_u32_e32 v79, 0x8000, v80
	v_perm_b32 v79, v41, v79, s33
	s_nop 2
	v_add_u32_e32 v41, 0x8000, v75
	v_add_u32_e32 v74, 0x8000, v74
	v_perm_b32 v74, v41, v74, s33
	v_add_u32_e32 v41, 0x8000, v77
	v_add_u32_e32 v75, 0x8000, v76
	v_perm_b32 v75, v41, v75, s33
	global_store_dwordx2 v[46:47], v[74:75], off offset:160
	ds_read_b128 v[74:77], v73 offset:30208
	ds_read_b128 v[82:85], v73 offset:30272
	global_store_dwordx2 v[44:45], v[78:79], off offset:160
	s_waitcnt lgkmcnt(1)
	v_mfma_f32_16x16x32_bf16 v[78:81], v[74:77], v[26:29], 0
	v_mfma_f32_16x16x32_bf16 v[74:77], v[74:77], v[30:33], 0
	s_waitcnt lgkmcnt(0)
	v_mfma_f32_16x16x32_bf16 v[78:81], v[82:85], v[18:21], v[78:81]
	v_mfma_f32_16x16x32_bf16 v[74:77], v[82:85], v[22:25], v[74:77]
	ds_read_b128 v[82:85], v73 offset:30336
	s_waitcnt lgkmcnt(0)
	v_mfma_f32_16x16x32_bf16 v[78:81], v[82:85], v[10:13], v[78:81]
	v_mfma_f32_16x16x32_bf16 v[74:77], v[82:85], v[14:17], v[74:77]
	ds_read_b128 v[82:85], v73 offset:30400
	s_waitcnt lgkmcnt(0)
	v_mfma_f32_16x16x32_bf16 v[78:81], v[82:85], v[6:9], v[78:81]
	s_nop 7
	v_add_u32_e32 v41, 0x8000, v79
	v_mfma_f32_16x16x32_bf16 v[74:77], v[82:85], v[2:5], v[74:77]
	v_add_u32_e32 v78, 0x8000, v78
	v_perm_b32 v78, v41, v78, s33
	v_add_u32_e32 v41, 0x8000, v81
	v_add_u32_e32 v79, 0x8000, v80
	v_perm_b32 v79, v41, v79, s33
	s_nop 2
	v_add_u32_e32 v41, 0x8000, v75
	v_add_u32_e32 v74, 0x8000, v74
	v_perm_b32 v74, v41, v74, s33
	v_add_u32_e32 v41, 0x8000, v77
	v_add_u32_e32 v75, 0x8000, v76
	v_perm_b32 v75, v41, v75, s33
	global_store_dwordx2 v[46:47], v[74:75], off offset:192
	ds_read_b128 v[74:77], v73 offset:34560
	s_waitcnt lgkmcnt(0)
	v_mfma_f32_16x16x32_bf16 v[26:29], v[74:77], v[26:29], 0
	global_store_dwordx2 v[44:45], v[78:79], off offset:192
	v_mfma_f32_16x16x32_bf16 v[30:33], v[74:77], v[30:33], 0
	ds_read_b128 v[74:77], v73 offset:34624
	s_waitcnt lgkmcnt(0)
	v_mfma_f32_16x16x32_bf16 v[18:21], v[74:77], v[18:21], v[26:29]
	s_nop 2
	ds_read_b128 v[26:29], v73 offset:34688
	s_waitcnt lgkmcnt(0)
	v_mfma_f32_16x16x32_bf16 v[10:13], v[26:29], v[10:13], v[18:21]
	s_nop 2
	ds_read_b128 v[18:21], v73 offset:34752
	v_mfma_f32_16x16x32_bf16 v[22:25], v[74:77], v[22:25], v[30:33]
	v_mfma_f32_16x16x32_bf16 v[14:17], v[26:29], v[14:17], v[22:25]
	s_waitcnt lgkmcnt(0)
	v_mfma_f32_16x16x32_bf16 v[6:9], v[18:21], v[6:9], v[10:13]
	v_mfma_f32_16x16x32_bf16 v[2:5], v[18:21], v[2:5], v[14:17]
	s_nop 6
	v_add_u32_e32 v7, 0x8000, v7
	v_add_u32_e32 v6, 0x8000, v6
	v_add_u32_e32 v3, 0x8000, v3
	v_add_u32_e32 v2, 0x8000, v2
	v_perm_b32 v6, v7, v6, s33
	v_add_u32_e32 v7, 0x8000, v9
	v_add_u32_e32 v8, 0x8000, v8
	v_perm_b32 v2, v3, v2, s33
	v_add_u32_e32 v3, 0x8000, v5
	v_add_u32_e32 v4, 0x8000, v4
	v_perm_b32 v7, v7, v8, s33
	v_perm_b32 v3, v3, v4, s33
	global_store_dwordx2 v[44:45], v[6:7], off offset:224
	global_store_dwordx2 v[46:47], v[2:3], off offset:224
	s_and_saveexec_b64 s[22:23], vcc
	s_cbranch_execz .LBB0_375
	s_add_i32 s24, 0, 0x600
	v_mov_b32_e32 v2, 0
	s_mov_b32 s25, 0
